# scan loader: nt (streaming) hint on the 8 expert-weight tile loads
# baseline (speedup 1.0000x reference)
; __device__ __forceinline__ void p4_scan(const Args& a, const Frame& F) {
;     ...
;             auto prefetch = [&](int ci) {
;                 const int base = chunk_base(ci);
; #pragma unroll
;                 for (int i = 0; i < 8; ++i) { const int p = ht + 256 * i, row = p >> 4, c16 = p & 15; const int tok = base + (dir ? 127 - row : row);
;                     pq[i] = *(const u32x4*)(QKC + (size_t)tok * 1024 + h * 128 + c16 * 8); pk[i] = *(const u32x4*)(QKC + (size_t)tok * 1024 + 512 + h * 128 + c16 * 8); }
;     ...
;             auto conv_load = [&](int it) {
;                 const float* cW; int cN, cn;
;                 if (it < 32768) { const int e = it >> 10, sb = it & 1023; ck0 = (sb >> 6) * 64; cn = (sb & 63) * 32 + (lane & 31); cN = 2048; cW = a.in[IN_W1] + (size_t)e * 1024 * 2048; cD = (bf16*)(a.ws + WS_W1T);
;                     const int up = cn >= 1024, nn = cn & 1023; crow = e * 2048 + (nn >> 7) * 256 + up * 128 + (nn & 127); }
;                 else { const int it2 = it - 32768, e = it2 >> 9, sb = it2 & 511; ck0 = (sb >> 5) * 64; cn = (sb & 31) * 32 + (lane & 31); cN = 1024; cW = a.in[IN_W2] + (size_t)e * 1024 * 1024; cD = (bf16*)(a.ws + WS_W2T); crow = e * 1024 + cn; }
; #pragma unroll
;                 for (int i = 0; i < 32; ++i) cv[i] = cW[(size_t)(ck0 + (lane >> 5) + 2 * i) * cN + cn];
;             };
.LBB0_490:
	v_and_b32_e32 v82, 0x3c0, v9
	v_and_b32_e32 v206, 7, v252
	v_lshlrev_b32_e32 v206, 2, v206
	v_and_b32_e32 v207, 31, v252
	v_sub_u32_e32 v206, v206, v207
	v_and_b32_e32 v207, 0x38, v252
	v_add_u32_e32 v12, v8, v206
	v_add_u32_e32 v14, v82, v207
	v_mul_u32_u24_e32 v14, s54, v14
	v_add_u32_e32 v12, v12, v14
	v_mov_b32_e32 v13, v145
	v_lshl_add_u64 v[12:13], v[12:13], 2, s[56:57]
	global_load_dwordx4 v[174:177], v[12:13], off nt
	v_lshl_add_u64 v[12:13], s[54:55], 2, v[12:13]
	global_load_dwordx4 v[178:181], v[12:13], off nt
	v_lshl_add_u64 v[12:13], s[54:55], 2, v[12:13]
	global_load_dwordx4 v[182:185], v[12:13], off nt
	v_lshl_add_u64 v[12:13], s[54:55], 2, v[12:13]
	global_load_dwordx4 v[138:141], v[12:13], off nt
	v_lshl_add_u64 v[12:13], s[54:55], 2, v[12:13]
	global_load_dwordx4 v[148:151], v[12:13], off nt
	v_lshl_add_u64 v[12:13], s[54:55], 2, v[12:13]
	global_load_dwordx4 v[198:201], v[12:13], off nt
	v_lshl_add_u64 v[12:13], s[54:55], 2, v[12:13]
	global_load_dwordx4 v[202:205], v[12:13], off nt
	v_lshl_add_u64 v[12:13], s[54:55], 2, v[12:13]
	global_load_dwordx4 v[210:213], v[12:13], off nt
	s_lshl_b32 s44, s44, 1
	s_add_u32 s54, s20, s44
	s_addc_u32 s55, s21, 0
	s_lshl_b32 s33, s33, 1
	s_add_u32 s54, s54, s33
	s_addc_u32 s55, s55, 0
	v_mov_b32_e32 v87, v145
	v_lshl_add_u64 v[86:87], s[54:55], 0, v[86:87]
	s_add_i32 s54, s34, s35
	v_mov_b64_e32 v[8:9], s[38:39]
	s_add_i32 s33, 0, 0x23430
	v_mad_i64_i32 v[88:89], s[34:35], v88, s95, v[8:9]
	v_mad_i64_i32 v[90:91], s[34:35], v90, s95, v[8:9]
	s_add_i32 s54, s54, 0x10000
	v_add_u32_e32 v12, s33, v11
	s_lshl_b32 s33, s58, 13
	s_xor_b32 s34, s54, 0x80
	s_add_u32 s54, s16, s44
	v_add_u32_e32 v11, s89, v11
	s_addc_u32 s55, s17, 0
	v_lshl_add_u64 v[92:93], s[54:55], 0, v[144:145]
	s_mov_b32 s44, 0
	v_mov_b32_e32 v136, 0
	v_add_u32_e32 v134, v12, v10
	v_add_u32_e32 v135, v11, v10
	v_add_u32_e32 v214, s34, v96
	v_ashrrev_i32_e32 v215, 31, v214
	v_lshlrev_b64 v[214:215], 11, v[214:215]
	v_lshl_add_u64 v[214:215], v[92:93], 0, v[214:215]
	global_load_dwordx4 v[220:223], v[214:215], off offset:1024
	v_add_u32_e32 v214, s34, v97
	v_ashrrev_i32_e32 v215, 31, v214
	v_lshlrev_b64 v[214:215], 11, v[214:215]
	v_lshl_add_u64 v[214:215], v[92:93], 0, v[214:215]
	global_load_dwordx4 v[224:227], v[214:215], off offset:1024
	v_add_u32_e32 v214, s34, v98
	v_ashrrev_i32_e32 v215, 31, v214
	v_lshlrev_b64 v[214:215], 11, v[214:215]
	v_lshl_add_u64 v[214:215], v[92:93], 0, v[214:215]
	global_load_dwordx4 v[228:231], v[214:215], off offset:1024
	v_add_u32_e32 v214, s34, v99
	v_ashrrev_i32_e32 v215, 31, v214
	v_lshlrev_b64 v[214:215], 11, v[214:215]
	v_lshl_add_u64 v[214:215], v[92:93], 0, v[214:215]
	global_load_dwordx4 v[232:235], v[214:215], off offset:1024
	v_add_u32_e32 v214, s34, v100
	v_ashrrev_i32_e32 v215, 31, v214
	v_lshlrev_b64 v[214:215], 11, v[214:215]
	v_lshl_add_u64 v[214:215], v[92:93], 0, v[214:215]
	global_load_dwordx4 v[236:239], v[214:215], off offset:1024
	v_add_u32_e32 v214, s34, v101
	v_ashrrev_i32_e32 v215, 31, v214
	v_lshlrev_b64 v[214:215], 11, v[214:215]
	v_lshl_add_u64 v[214:215], v[92:93], 0, v[214:215]
	global_load_dwordx4 v[240:243], v[214:215], off offset:1024
	v_add_u32_e32 v214, s34, v102
	v_ashrrev_i32_e32 v215, 31, v214
	v_lshlrev_b64 v[214:215], 11, v[214:215]
	v_lshl_add_u64 v[214:215], v[92:93], 0, v[214:215]
	global_load_dwordx4 v[244:247], v[214:215], off offset:1024
	v_add_u32_e32 v214, s34, v103
	v_ashrrev_i32_e32 v215, 31, v214
	v_lshlrev_b64 v[214:215], 11, v[214:215]
	v_lshl_add_u64 v[214:215], v[92:93], 0, v[214:215]
	global_load_dwordx4 v[248:251], v[214:215], off offset:1024
	v_add_u32_e32 v214, s34, v96
	v_ashrrev_i32_e32 v215, 31, v214
	v_lshlrev_b64 v[214:215], 11, v[214:215]
	v_lshl_add_u64 v[214:215], v[92:93], 0, v[214:215]
	global_load_dwordx4 v[16:19], v[214:215], off
	v_add_u32_e32 v214, s34, v97
	v_ashrrev_i32_e32 v215, 31, v214
	v_lshlrev_b64 v[214:215], 11, v[214:215]
	v_lshl_add_u64 v[214:215], v[92:93], 0, v[214:215]
	global_load_dwordx4 v[20:23], v[214:215], off
	v_add_u32_e32 v214, s34, v98
	v_ashrrev_i32_e32 v215, 31, v214
	v_lshlrev_b64 v[214:215], 11, v[214:215]
	v_lshl_add_u64 v[214:215], v[92:93], 0, v[214:215]
	global_load_dwordx4 v[24:27], v[214:215], off
	v_add_u32_e32 v214, s34, v99
	v_ashrrev_i32_e32 v215, 31, v214
	v_lshlrev_b64 v[214:215], 11, v[214:215]
	v_lshl_add_u64 v[214:215], v[92:93], 0, v[214:215]
	global_load_dwordx4 v[28:31], v[214:215], off
	v_add_u32_e32 v214, s34, v100
	v_ashrrev_i32_e32 v215, 31, v214
	v_lshlrev_b64 v[214:215], 11, v[214:215]
	v_lshl_add_u64 v[214:215], v[92:93], 0, v[214:215]
	global_load_dwordx4 v[32:35], v[214:215], off
	v_add_u32_e32 v214, s34, v101
	v_ashrrev_i32_e32 v215, 31, v214
	v_lshlrev_b64 v[214:215], 11, v[214:215]
	v_lshl_add_u64 v[214:215], v[92:93], 0, v[214:215]
	global_load_dwordx4 v[36:39], v[214:215], off
	v_add_u32_e32 v214, s34, v102
	v_ashrrev_i32_e32 v215, 31, v214
	v_lshlrev_b64 v[214:215], 11, v[214:215]
	v_lshl_add_u64 v[214:215], v[92:93], 0, v[214:215]
	global_load_dwordx4 v[40:43], v[214:215], off
	v_add_u32_e32 v214, s34, v103
	v_ashrrev_i32_e32 v215, 31, v214
	v_lshlrev_b64 v[214:215], 11, v[214:215]
	v_lshl_add_u64 v[214:215], v[92:93], 0, v[214:215]
	global_load_dwordx4 v[44:47], v[214:215], off
	s_waitcnt vmcnt(8)
	s_branch .LBB0_492

; #define LAS __attribute__((address_space(3)))
; __device__ __forceinline__ float bflo(unsigned w) { return __uint_as_float(w << 16); }
; __device__ __forceinline__ void p4_scan(const Args& a, const Frame& F) {
;     ...
;             auto commitQ = [&]() {
; #pragma unroll
;                 for (int i = 0; i < 8; ++i) { const int p = ht + 256 * i, row = p >> 4, c16 = p & 15; *(LAS u32x4*)(L + S_QS + row * SP + c16 * 16) = pq[i]; } };
;             auto commitV = [&](float mprev, int vabuf) {
; #pragma unroll
;                 for (int i = 0; i < 2; ++i) { const int p = ht + 256 * i, row = p >> 2, cc = p & 3; const unsigned wv[4] = {pv[i].x, pv[i].y, pv[i].z, pv[i].w};
;                     const float av = __expf(pga[i] - fmaxf(ppx, mprev));
; #pragma unroll
;                     for (int j = 0; j < 4; ++j) { const unsigned sc2 = pg8::cvt_pk_bf16(av * bflo(wv[j]), av * bfhi(wv[j]));
;                         *(LAS bf16*)(L + S_VT + (cc * 8 + 2 * j) * SP + row * 2) = (bf16)(wv[j] & 0xffffu); *(LAS bf16*)(L + S_VT + (cc * 8 + 2 * j + 1) * SP + row * 2) = (bf16)(wv[j] >> 16);
;                         *(LAS bf16*)(L + vabuf + (cc * 8 + 2 * j) * SP + row * 2) = (bf16)(sc2 & 0xffffu); *(LAS bf16*)(L + vabuf + (cc * 8 + 2 * j + 1) * SP + row * 2) = (bf16)(sc2 >> 16); }
;                     if (cc == 0) *(LAS bf16*)(L + vabuf + 32 * SP + row * 2) = (bf16)f2bf(av); }
; #pragma unroll
;                 for (int i = 0; i < 2; ++i) { const int idx = ht + 256 * i; if (idx < 384) { const int row = idx & 127, arr = idx >> 7; *(LAS float*)(L + S_GL + arr * 512 + row * 4) = pgl[i]; } }
;             };
;             prefetch(0);
;             LDS_BARRIER();
;             commitK(S_K0); commitQ(); commitV(0.f, S_VA0);
;             float btot = pbt, pmx = ppx;
;             LDS_BARRIER();
;             const int lw = blk * 4 + (w - 4);
;             float cv[32]; bf16* cD = nullptr; int ck0 = 0, crow = 0;
;             auto conv_load = [&](int it) {
;                 const float* cW; int cN, cn;
;                 if (it < 32768) { const int e = it >> 10, sb = it & 1023; ck0 = (sb >> 6) * 64; cn = (sb & 63) * 32 + (lane & 31); cN = 2048; cW = a.in[IN_W1] + (size_t)e * 1024 * 2048; cD = (bf16*)(a.ws + WS_W1T);
;                     const int up = cn >= 1024, nn = cn & 1023; crow = e * 2048 + (nn >> 7) * 256 + up * 128 + (nn & 127); }
.LBB0_502:
	s_cmp_ge_u32 s35, 48
	s_cselect_b32 s56, 0, s56
	v_and_b32_e32 v82, 0x3c0, v48
	v_max_f32_e32 v49, v136, v136
	v_max_f32_e32 v50, v85, v85
	v_max_f32_e32 v49, v50, v49
	v_add_f32_e32 v136, v84, v49
	v_add_u32_e32 v48, v144, v206
	v_add_u32_e32 v50, v82, v207
	v_mul_u32_u24_e32 v50, s56, v50
	v_add_u32_e32 v48, v48, v50
	v_mov_b32_e32 v49, v145
	v_lshl_add_u64 v[48:49], v[48:49], 2, s[58:59]
	global_load_dwordx4 v[174:177], v[48:49], off nt
	v_lshl_add_u64 v[48:49], s[56:57], 2, v[48:49]
	global_load_dwordx4 v[178:181], v[48:49], off nt
	v_lshl_add_u64 v[48:49], s[56:57], 2, v[48:49]
	global_load_dwordx4 v[182:185], v[48:49], off nt
	v_lshl_add_u64 v[48:49], s[56:57], 2, v[48:49]
	global_load_dwordx4 v[138:141], v[48:49], off nt
	v_lshl_add_u64 v[48:49], s[56:57], 2, v[48:49]
	global_load_dwordx4 v[148:151], v[48:49], off nt
	v_lshl_add_u64 v[48:49], s[56:57], 2, v[48:49]
	global_load_dwordx4 v[198:201], v[48:49], off nt
	v_lshl_add_u64 v[48:49], s[56:57], 2, v[48:49]
	global_load_dwordx4 v[202:205], v[48:49], off nt
	v_lshl_add_u64 v[48:49], s[56:57], 2, v[48:49]
	global_load_dwordx4 v[210:213], v[48:49], off nt
	s_waitcnt lgkmcnt(0)
	s_barrier
	s_waitcnt vmcnt(16)
	ds_write_b128 v119, v[16:19]
	ds_write_b128 v120, v[20:23]
	ds_write_b128 v121, v[24:27]
	ds_write_b128 v122, v[28:31]
	ds_write_b128 v123, v[32:35]
	ds_write_b128 v124, v[36:39]
	ds_write_b128 v125, v[40:43]
	ds_write_b128 v126, v[44:47]
	v_add_u32_e32 v214, s98, v96
	v_ashrrev_i32_e32 v215, 31, v214
	v_lshlrev_b64 v[214:215], 11, v[214:215]
	v_lshl_add_u64 v[214:215], v[92:93], 0, v[214:215]
	global_load_dwordx4 v[16:19], v[214:215], off
	v_add_u32_e32 v214, s98, v97
	v_ashrrev_i32_e32 v215, 31, v214
	v_lshlrev_b64 v[214:215], 11, v[214:215]
	v_lshl_add_u64 v[214:215], v[92:93], 0, v[214:215]
	global_load_dwordx4 v[20:23], v[214:215], off
	v_add_u32_e32 v214, s98, v98
	v_ashrrev_i32_e32 v215, 31, v214
	v_lshlrev_b64 v[214:215], 11, v[214:215]
	v_lshl_add_u64 v[214:215], v[92:93], 0, v[214:215]
	global_load_dwordx4 v[24:27], v[214:215], off
	v_add_u32_e32 v214, s98, v99
	v_ashrrev_i32_e32 v215, 31, v214
	v_lshlrev_b64 v[214:215], 11, v[214:215]
	v_lshl_add_u64 v[214:215], v[92:93], 0, v[214:215]
	global_load_dwordx4 v[28:31], v[214:215], off
	v_add_u32_e32 v214, s98, v100
	v_ashrrev_i32_e32 v215, 31, v214
	v_lshlrev_b64 v[214:215], 11, v[214:215]
	v_lshl_add_u64 v[214:215], v[92:93], 0, v[214:215]
	global_load_dwordx4 v[32:35], v[214:215], off
	v_add_u32_e32 v214, s98, v101
	v_ashrrev_i32_e32 v215, 31, v214
	v_lshlrev_b64 v[214:215], 11, v[214:215]
	v_lshl_add_u64 v[214:215], v[92:93], 0, v[214:215]
	global_load_dwordx4 v[36:39], v[214:215], off
	v_add_u32_e32 v214, s98, v102
	v_ashrrev_i32_e32 v215, 31, v214
	v_lshlrev_b64 v[214:215], 11, v[214:215]
	v_lshl_add_u64 v[214:215], v[92:93], 0, v[214:215]
	global_load_dwordx4 v[40:43], v[214:215], off
	v_add_u32_e32 v214, s98, v103
	v_ashrrev_i32_e32 v215, 31, v214
	v_lshlrev_b64 v[214:215], 11, v[214:215]
	v_lshl_add_u64 v[214:215], v[92:93], 0, v[214:215]
	global_load_dwordx4 v[44:47], v[214:215], off
	v_max_f32_e32 v192, v95, v95
	v_max_f32_e32 v192, v192, v136
	v_sub_f32_e32 v193, v172, v192
	v_mul_f32_e32 v193, 0x3fb8aa3b, v193
	v_exp_f32_e32 v193, v193
	s_and_b64 s[54:55], s[54:55], exec
	v_lshlrev_b32_e32 v194, 16, v12
	v_and_b32_e32 v195, 0xffff0000, v12
	s_cselect_b32 s44, 0x1de20, s92
	v_mul_f32_e32 v194, v193, v194
	v_mul_f32_e32 v195, v193, v195
	v_cvt_pk_bf16_f32 v194, v194, v195
	v_add_u32_e32 v195, v128, v129
	s_add_i32 s44, s44, 0
	ds_write_b16 v127, v12
	ds_write_b16_d16_hi v195, v12 offset:272
	v_add_u32_e32 v12, s44, v129
	v_add_u32_e32 v196, v12, v118
	ds_write_b16 v196, v194
	ds_write_b16_d16_hi v196, v194 offset:272
	v_lshlrev_b32_e32 v194, 16, v13
	v_mul_f32_e32 v194, v193, v194
	v_and_b32_e32 v197, 0xffff0000, v13
	v_mul_f32_e32 v197, v193, v197
	v_cvt_pk_bf16_f32 v194, v194, v197
	ds_write_b16 v195, v13 offset:544
	ds_write_b16_d16_hi v195, v13 offset:816
	ds_write_b16 v196, v194 offset:544
	ds_write_b16_d16_hi v196, v194 offset:816
	v_lshlrev_b32_e32 v13, 16, v14
	v_mul_f32_e32 v13, v193, v13
	v_and_b32_e32 v194, 0xffff0000, v14
	v_mul_f32_e32 v194, v193, v194
	v_cvt_pk_bf16_f32 v13, v13, v194
	ds_write_b16 v195, v14 offset:1088
	ds_write_b16_d16_hi v195, v14 offset:1360
	ds_write_b16 v196, v13 offset:1088
	ds_write_b16_d16_hi v196, v13 offset:1360
	v_lshlrev_b32_e32 v13, 16, v15
	v_mul_f32_e32 v13, v193, v13
	v_and_b32_e32 v14, 0xffff0000, v15
	v_mul_f32_e32 v14, v193, v14
	v_cvt_pk_bf16_f32 v13, v13, v14
	ds_write_b16 v195, v15 offset:1632
	ds_write_b16_d16_hi v195, v15 offset:1904
	ds_write_b16 v196, v13 offset:1632
	ds_write_b16_d16_hi v196, v13 offset:1904
	s_and_saveexec_b64 s[54:55], s[10:11]
	v_bfe_u32 v13, v193, 16, 1
	v_add3_u32 v13, v193, v13, s93
	v_add_u32_e32 v14, s44, v118
	ds_write_b16_d16_hi v14, v13 offset:8704
	s_or_b64 exec, exec, s[54:55]
	v_sub_f32_e32 v13, v171, v192
	v_mul_f32_e32 v13, 0x3fb8aa3b, v13
	v_exp_f32_e32 v13, v13
	v_lshlrev_b32_e32 v14, 16, v8
	v_and_b32_e32 v15, 0xffff0000, v8
	v_mul_f32_e32 v14, v13, v14
	v_mul_f32_e32 v15, v13, v15
	v_cvt_pk_bf16_f32 v14, v14, v15
	ds_write_b16 v131, v8
	ds_write_b16_d16_hi v132, v8 offset:272
	v_add_u32_e32 v8, v12, v130
	v_lshlrev_b32_e32 v12, 16, v9
	ds_write_b16 v8, v14
	ds_write_b16_d16_hi v8, v14 offset:272
	v_mul_f32_e32 v12, v13, v12
	v_and_b32_e32 v14, 0xffff0000, v9
	v_mul_f32_e32 v14, v13, v14
	v_cvt_pk_bf16_f32 v12, v12, v14
	ds_write_b16 v132, v9 offset:544
	ds_write_b16_d16_hi v132, v9 offset:816
	ds_write_b16 v8, v12 offset:544
	ds_write_b16_d16_hi v8, v12 offset:816
	v_lshlrev_b32_e32 v9, 16, v10
	v_mul_f32_e32 v9, v13, v9
	v_and_b32_e32 v12, 0xffff0000, v10
	v_mul_f32_e32 v12, v13, v12
	v_cvt_pk_bf16_f32 v9, v9, v12
	ds_write_b16 v132, v10 offset:1088
	ds_write_b16_d16_hi v132, v10 offset:1360
	ds_write_b16 v8, v9 offset:1088
	ds_write_b16_d16_hi v8, v9 offset:1360
	v_lshlrev_b32_e32 v9, 16, v11
	v_mul_f32_e32 v9, v13, v9
	v_and_b32_e32 v10, 0xffff0000, v11
	v_mul_f32_e32 v10, v13, v10
	v_cvt_pk_bf16_f32 v9, v9, v10
	ds_write_b16 v132, v11 offset:1632
	ds_write_b16_d16_hi v132, v11 offset:1904
	ds_write_b16 v8, v9 offset:1632
	ds_write_b16_d16_hi v8, v9 offset:1904
	s_and_saveexec_b64 s[54:55], s[10:11]
	s_cbranch_execnz .LBB0_507
	s_or_b64 exec, exec, s[54:55]
	s_and_saveexec_b64 s[54:55], s[6:7]
	s_cbranch_execnz .LBB0_508
